# v028-clamp-free-softplus-packed-readlane
# speedup vs baseline: 1.0995x; 1.0053x over previous
.LBB4_8:
	s_or_b64 exec, exec, s[2:3]
	s_movk_i32 s17, 0x61a8
	v_cmp_gt_i32_e32 vcc, s17, v64
	s_waitcnt lgkmcnt(0)
	s_barrier
	s_and_saveexec_b64 s[2:3], vcc
	s_cbranch_execz .LBB4_73
	s_load_dwordx4 s[4:7], s[0:1], 0x30
	s_load_dwordx2 s[2:3], s[0:1], 0x40
	v_and_b32_e32 v1, 63, v0
	s_waitcnt vmcnt(3)
	v_mov_b32_e32 v2, 0x3e020821
	v_cmp_gt_u32_e64 s[0:1], 32, v1
	v_mov_b32_e32 v68, 0xffff
	v_cmp_ne_u32_e32 vcc, 0, v54
	v_cndmask_b32_e64 v67, v2, 0, s[0:1]
	s_waitcnt vmcnt(0)
	v_lshrrev_b32_e32 v2, 16, v55
	v_lshrrev_b32_e32 v0, 1, v0
	v_mov_b32_e32 v3, 0x7a00
	v_ashrrev_i32_e32 v65, 31, v64
	v_lshlrev_b32_e32 v52, 2, v1
	v_cndmask_b32_e32 v95, v68, v2, vcc
	s_lshl_b32 s12, s10, 2
	v_lshlrev_b32_e32 v2, 4, v1
	v_and_or_b32 v70, v0, 16, v3
	v_lshlrev_b32_e32 v73, 1, v1
	v_lshlrev_b64 v[0:1], 8, v[64:65]
	v_mov_b32_e32 v53, 0
	v_or_b32_e32 v0, v0, v52
	s_ashr_i32 s13, s12, 31
	s_mov_b32 s11, 0
	v_add_u32_e32 v69, 0x3200, v2
	v_add_u32_e32 v71, 0x5200, v2
	v_add_u32_e32 v72, 0x7200, v2
	s_waitcnt lgkmcnt(0)
	v_lshl_add_u64 v[60:61], s[6:7], 0, v[52:53]
	s_mov_b64 s[60:61], s[6:7]
	v_lshl_add_u64 v[62:63], s[2:3], 0, v[0:1]
	s_lshl_b64 s[6:7], s[12:13], 8
	s_mov_b64 s[14:15], 0
	s_movk_i32 s13, 0x61a7
	v_mov_b32_e32 v65, 0xc0669d92
	s_mov_b32 s22, 0xc1c00000
	v_mov_b32_e32 v74, 0x41c00000
	v_mov_b32_e32 v75, 0xbfb8aa3b
	v_mov_b32_e32 v76, 0xc1b69213
	v_mov_b32_e32 v77, 0xc228283a
	v_mov_b32_e32 v78, 0xc275076b
	s_mov_b32 s16, 0x3e0a9555
	v_mov_b32_e32 v79, v52
	v_readfirstlane_b32 s94, v64
	s_nop 3
	v_lshlrev_b32_e32 v124, 4, v66
	s_lshl_b32 s95, s94, 8
	s_add_u32 s62, s2, s95
	s_addc_u32 s63, s3, 0
	v_add_u32_e32 v125, 64, v79
	v_and_b32_e32 v125, 0xfc, v125
	s_mov_b32 s64, 0x5040100
	s_branch .LBB4_11

.Lprio_e1_done:
	s_mov_b32 s93, s94
	s_add_u32 s94, s94, 0x1000
	s_cmp_lt_u32 s94, 0x61a8
	s_cselect_b32 s95, s94, s93
	s_lshl_b32 s95, s95, 9
	s_add_u32 s56, s8, s95
	s_addc_u32 s57, s9, 0
	ds_bpermute_b32 v126, v125, v51
	v_sub_f32_e32 v39, v48, v67
	v_fmamk_f32 v32, v39, 0x4297576a, v65
	v_fmamk_f32 v33, v39, 0x4297576a, v76
	v_med3_f32 v35, v32, s22, v74
	v_med3_f32 v37, v33, s22, v74
	v_mul_f32_e64 v32, v35, -v35
	v_fmamk_f32 v34, v35, 0x4019be61, v75
	v_mul_f32_e64 v33, v37, -v37
	v_fmamk_f32 v35, v35, 0xc019be61, v75
	v_exp_f32_e32 v32, v32
	v_exp_f32_e32 v33, v33
	v_exp_f32_e32 v36, v35
	v_fmamk_f32 v35, v37, 0x4019be61, v75
	v_exp_f32_e32 v34, v34
	v_exp_f32_e32 v35, v35
	v_fmamk_f32 v37, v37, 0xc019be61, v75
	v_exp_f32_e32 v37, v37
	v_pk_mul_f32 v[32:33], v[48:49], v[32:33] op_sel:[1,0]
	ds_read_b128 v[28:31], v69
	ds_read_b128 v[24:27], v69 offset:1024
	ds_read_b128 v[20:23], v69 offset:2048
	ds_read_b128 v[16:19], v69 offset:3072
	ds_read_b128 v[0:3], v70
	ds_read_b128 v[4:7], v70 offset:32
	ds_read_b128 v[8:11], v70 offset:64
	ds_read_b128 v[12:15], v70 offset:96
	v_pk_mul_f32 v[44:45], v[34:35], v[32:33]
	v_pk_mul_f32 v[34:35], v[34:35], s[16:17] op_sel_hi:[1,0]
	v_mov_b32_e32 v99, v80
	v_fmamk_f32 v38, v39, 0x4297576a, v77
	v_fmamk_f32 v39, v39, 0x4297576a, v78
	v_pk_mul_f32 v[46:47], v[34:35], v[44:45]
	v_pk_mul_f32 v[34:35], v[34:35], s[16:17] op_sel_hi:[1,0]
	v_pk_mul_f32 v[80:81], v[36:37], v[32:33]
	v_pk_mul_f32 v[36:37], v[36:37], s[16:17] op_sel_hi:[1,0]
	v_med3_f32 v41, v38, s22, v74
	v_med3_f32 v43, v39, s22, v74
	v_pk_mul_f32 v[58:59], v[34:35], v[46:47]
	v_pk_mul_f32 v[34:35], v[34:35], s[16:17] op_sel_hi:[1,0]
	v_pk_mul_f32 v[82:83], v[36:37], v[80:81]
	v_pk_mul_f32 v[36:37], v[36:37], s[16:17] op_sel_hi:[1,0]
	v_mul_f32_e64 v38, v41, -v41
	v_fmamk_f32 v40, v41, 0x4019be61, v75
	v_mul_f32_e64 v39, v43, -v43
	v_fmamk_f32 v41, v41, 0xc019be61, v75
	v_pk_mul_f32 v[34:35], v[34:35], v[58:59]
	v_pk_mul_f32 v[36:37], v[36:37], v[82:83]
	v_exp_f32_e32 v38, v38
	v_exp_f32_e32 v39, v39
	v_exp_f32_e32 v42, v41
	v_fmamk_f32 v41, v43, 0x4019be61, v75
	v_cvt_pk_f16_f32 v56, v44, v46
	v_cvt_pk_f16_f32 v54, v36, v82
	v_cvt_pk_f16_f32 v57, v58, v34
	v_cvt_pk_f16_f32 v55, v80, v32
	v_exp_f32_e32 v40, v40
	v_exp_f32_e32 v41, v41
	s_waitcnt lgkmcnt(0)
	v_mfma_f32_32x32x16_f16 v[0:15], v[28:31], v[54:57], v[0:15]
	v_mul_f32_e64 v38, v49, v38
	v_mul_f32_e64 v39, v49, v39
	v_fmamk_f32 v43, v43, 0xc019be61, v75
	v_mul_f32_e64 v84, v40, v38
	v_mul_f32_e64 v85, v41, v39
	v_pk_mul_f32 v[40:41], v[40:41], s[16:17] op_sel_hi:[1,0]
	v_cvt_pk_f16_f32 v30, v45, v47
	v_pk_mul_f32 v[86:87], v[40:41], v[84:85]
	v_pk_mul_f32 v[28:29], v[40:41], s[16:17] op_sel_hi:[1,0]
	v_cvt_pk_f16_f32 v31, v59, v35
	v_pk_mul_f32 v[40:41], v[28:29], v[86:87]
	v_pk_mul_f32 v[28:29], v[28:29], s[16:17] op_sel_hi:[1,0]
	v_exp_f32_e32 v43, v43
	v_pk_mul_f32 v[88:89], v[28:29], v[40:41]
	v_cvt_pk_f16_f32 v28, v37, v83
	v_cvt_pk_f16_f32 v29, v81, v33
	v_pk_mul_f32 v[36:37], v[42:43], v[38:39]
	v_pk_mul_f32 v[42:43], v[42:43], s[16:17] op_sel_hi:[1,0]
	v_mfma_f32_32x32x16_f16 v[0:15], v[24:27], v[28:31], v[0:15]
	v_mul_f32_e64 v32, v42, v36
	v_mul_f32_e64 v33, v43, v37
	v_mul_f32_e64 v24, v42, s16
	v_mul_f32_e64 v25, v43, s16
	v_cvt_pk_f16_f32 v26, v84, v86
	v_pk_mul_f32 v[34:35], v[24:25], v[32:33]
	v_cvt_pk_f16_f32 v27, v40, v88
	v_cvt_pk_f16_f32 v24, v34, v32
	v_cvt_pk_f16_f32 v25, v36, v38
	v_cvt_pk_f16_f32 v84, v85, v87
	v_cvt_pk_f16_f32 v82, v35, v33
	v_mfma_f32_32x32x16_f16 v[0:15], v[20:23], v[24:27], v[0:15]
	ds_read_b128 v[20:23], v69 offset:4096
	v_cvt_pk_f16_f32 v85, v41, v89
	v_cvt_pk_f16_f32 v83, v37, v39
	ds_read_b128 v[32:35], v70 offset:128
	ds_read_b128 v[36:39], v70 offset:160
	ds_read_b128 v[40:43], v70 offset:192
	ds_read_b128 v[44:47], v70 offset:224
	s_nop 0
	v_add_u32_e32 v64, s12, v64
	v_perm_b32 v127, v126, v51, s64
	s_nop 0
	v_readlane_b32 s70, v127, 0
	v_readlane_b32 s71, v127, 1
	v_readlane_b32 s72, v127, 2
	v_readlane_b32 s73, v127, 3
	v_readlane_b32 s74, v127, 4
	v_readlane_b32 s75, v127, 5
	v_readlane_b32 s76, v127, 6
	v_readlane_b32 s77, v127, 7
	v_readlane_b32 s78, v127, 8
	v_readlane_b32 s79, v127, 9
	v_readlane_b32 s80, v127, 10
	v_readlane_b32 s81, v127, 11
	v_readlane_b32 s82, v127, 12
	v_readlane_b32 s83, v127, 13
	v_readlane_b32 s84, v127, 14
	v_readlane_b32 s85, v127, 15
	s_pack_ll_b32_b16 s48, s70, 0
	v_mfma_f32_32x32x16_f16 v[0:15], v[16:19], v[82:85], v[0:15]
	ds_read_b128 v[16:19], v69 offset:5120
	s_nop 0
	s_lshl_b32 s48, s48, 8
	s_and_b32 s48, s48, 0xffff00
	s_pack_ll_b32_b16 s47, s71, 0
	s_add_u32 s48, s4, s48
	s_addc_u32 s49, s5, 0
	s_waitcnt lgkmcnt(1)
	v_mfma_f32_32x32x16_f16 v[32:47], v[20:23], v[54:57], v[32:47]
	ds_read_b128 v[20:23], v69 offset:6144
	s_lshl_b32 s47, s47, 8
	s_and_b32 s47, s47, 0xffff00
	s_pack_ll_b32_b16 s46, s72, 0
	s_pack_ll_b32_b16 s45, s73, 0
	s_pack_ll_b32_b16 s44, s74, 0
	s_pack_ll_b32_b16 s43, s75, 0
	s_waitcnt lgkmcnt(1)
	v_mfma_f32_32x32x16_f16 v[32:47], v[16:19], v[28:31], v[32:47]
	s_nop 0
	s_nop 0
	s_mov_b64 vcc, 0
	s_nop 0
	s_nop 0
	s_pack_ll_b32_b16 s3, s76, 0
	s_pack_ll_b32_b16 s2, s77, 0
	s_waitcnt lgkmcnt(0)
	v_mfma_f32_32x32x16_f16 v[32:47], v[20:23], v[24:27], v[32:47]
	s_nop 0
	s_nop 0
	s_pack_ll_b32_b16 s36, s78, 0
	s_pack_ll_b32_b16 s35, s79, 0
	s_pack_ll_b32_b16 s34, s80, 0
	s_pack_ll_b32_b16 s33, s81, 0
	s_pack_ll_b32_b16 s31, s82, 0
	s_pack_ll_b32_b16 s30, s83, 0
	s_pack_ll_b32_b16 s29, s84, 0
	s_pack_ll_b32_b16 s28, s85, 0
	s_pack_hh_b32_b16 s27, s70, 0
	s_pack_hh_b32_b16 s26, s71, 0
	s_pack_hh_b32_b16 s25, s72, 0
	s_pack_hh_b32_b16 s24, s73, 0
	s_pack_hh_b32_b16 s23, s74, 0
	s_pack_hh_b32_b16 s42, s75, 0
	s_pack_hh_b32_b16 s41, s76, 0
	s_pack_hh_b32_b16 s40, s77, 0
	s_pack_hh_b32_b16 s39, s78, 0
	s_pack_hh_b32_b16 s38, s79, 0
	s_pack_hh_b32_b16 s37, s80, 0
	s_pack_hh_b32_b16 s21, s81, 0
	s_pack_hh_b32_b16 s20, s82, 0
	s_pack_hh_b32_b16 s19, s83, 0
	s_pack_hh_b32_b16 s18, s84, 0
	s_pack_hh_b32_b16 s10, s85, 0
	ds_read_b128 v[16:19], v69 offset:7168
	s_nop 0
	global_load_dwordx4 v[56:59], v124, s[56:57]
	global_load_dword v80, v124, s[56:57] offset:24
	global_load_dword v51, v124, s[56:57] offset:-8
	global_load_dword v112, v79, s[48:49]
	s_add_u32 s48, s4, s47
	s_addc_u32 s49, s5, 0
	s_lshl_b32 s46, s46, 8
	s_and_b32 s46, s46, 0xffff00
	s_add_u32 s46, s4, s46
	s_addc_u32 s47, s5, 0
	s_lshl_b32 s45, s45, 8
	s_and_b32 s45, s45, 0xffff00
	global_load_dword v110, v79, s[48:49]
	global_load_dword v108, v79, s[46:47]
	s_add_u32 s46, s4, s45
	s_addc_u32 s47, s5, 0
	s_lshl_b32 s44, s44, 8
	s_and_b32 s44, s44, 0xffff00
	s_add_u32 s44, s4, s44
	s_addc_u32 s45, s5, 0
	s_lshl_b32 s43, s43, 8
	s_and_b32 s43, s43, 0xffff00
	global_load_dword v106, v79, s[46:47]
	global_load_dword v104, v79, s[44:45]
	s_add_u32 s44, s4, s43
	s_addc_u32 s45, s5, 0
	s_lshl_b32 s3, s3, 8
	s_and_b32 s3, s3, 0xffff00
	global_load_dword v102, v79, s[44:45]
	s_add_u32 s44, s4, s3
	s_addc_u32 s45, s5, 0
	s_lshl_b32 s2, s2, 8
	s_and_b32 s2, s2, 0xffff00
	s_add_u32 s2, s4, s2
	global_load_dword v100, v79, s[44:45]
	s_addc_u32 s3, s5, 0
	global_load_dword v114, v79, s[2:3]
	s_lshl_b32 s2, s36, 8
	s_and_b32 s2, s2, 0xffff00
	s_add_u32 s2, s4, s2
	s_addc_u32 s3, s5, 0
	global_load_dword v113, v79, s[2:3]
	s_lshl_b32 s2, s35, 8
	s_and_b32 s2, s2, 0xffff00
	s_add_u32 s2, s4, s2
	s_addc_u32 s3, s5, 0
	global_load_dword v111, v79, s[2:3]
	s_lshl_b32 s2, s34, 8
	s_and_b32 s2, s2, 0xffff00
	s_add_u32 s2, s4, s2
	s_addc_u32 s3, s5, 0
	global_load_dword v109, v79, s[2:3]
	s_lshl_b32 s2, s33, 8
	s_and_b32 s2, s2, 0xffff00
	s_add_u32 s2, s4, s2
	s_addc_u32 s3, s5, 0
	global_load_dword v107, v79, s[2:3]
	s_lshl_b32 s2, s31, 8
	s_and_b32 s2, s2, 0xffff00
	s_add_u32 s2, s4, s2
	s_addc_u32 s3, s5, 0
	global_load_dword v105, v79, s[2:3]
	s_lshl_b32 s2, s30, 8
	s_and_b32 s2, s2, 0xffff00
	s_add_u32 s2, s4, s2
	s_addc_u32 s3, s5, 0
	global_load_dword v103, v79, s[2:3]
	s_lshl_b32 s2, s29, 8
	s_and_b32 s2, s2, 0xffff00
	s_add_u32 s2, s4, s2
	s_addc_u32 s3, s5, 0
	global_load_dword v101, v79, s[2:3]
	s_lshl_b32 s2, s28, 8
	s_and_b32 s2, s2, 0xffff00
	s_add_u32 s2, s4, s2
	s_addc_u32 s3, s5, 0
	global_load_dword v98, v79, s[2:3]
	s_lshl_b32 s2, s27, 8
	s_and_b32 s2, s2, 0xffff00
	s_add_u32 s2, s4, s2
	s_addc_u32 s3, s5, 0
	global_load_dword v97, v79, s[2:3]
	s_lshl_b32 s2, s26, 8
	s_and_b32 s2, s2, 0xffff00
	s_add_u32 s2, s4, s2
	s_addc_u32 s3, s5, 0
	global_load_dword v96, v79, s[2:3]
	s_lshl_b32 s2, s25, 8
	s_and_b32 s2, s2, 0xffff00
	s_add_u32 s2, s4, s2
	s_addc_u32 s3, s5, 0
	global_load_dword v94, v79, s[2:3]
	s_lshl_b32 s2, s24, 8
	s_and_b32 s2, s2, 0xffff00
	s_add_u32 s2, s4, s2
	s_addc_u32 s3, s5, 0
	global_load_dword v91, v79, s[2:3]
	s_lshl_b32 s2, s23, 8
	s_and_b32 s2, s2, 0xffff00
	s_add_u32 s2, s4, s2
	s_addc_u32 s3, s5, 0
	global_load_dword v93, v79, s[2:3]
	s_lshl_b32 s2, s42, 8
	s_and_b32 s2, s2, 0xffff00
	s_add_u32 s2, s4, s2
	s_addc_u32 s3, s5, 0
	global_load_dword v90, v79, s[2:3]
	s_lshl_b32 s2, s41, 8
	s_and_b32 s2, s2, 0xffff00
	s_add_u32 s2, s4, s2
	s_addc_u32 s3, s5, 0
	global_load_dword v88, v79, s[2:3]
	s_lshl_b32 s2, s40, 8
	s_and_b32 s2, s2, 0xffff00
	s_add_u32 s2, s4, s2
	s_addc_u32 s3, s5, 0
	global_load_dword v86, v79, s[2:3]
	s_lshl_b32 s2, s39, 8
	s_and_b32 s2, s2, 0xffff00
	s_nop 0
	s_nop 0
	s_add_u32 s2, s4, s2
	s_waitcnt lgkmcnt(0)
	v_mfma_f32_32x32x16_f16 v[32:47], v[16:19], v[82:85], v[32:47]
	v_exp_f32_e32 v0, v0
	v_exp_f32_e32 v1, v1
	s_addc_u32 s3, s5, 0
	global_load_dword v85, v79, s[2:3]
	s_lshl_b32 s2, s38, 8
	s_and_b32 s2, s2, 0xffff00
	s_nop 0
	s_nop 0
	s_add_u32 s2, s4, s2
	v_exp_f32_e32 v6, v6
	v_exp_f32_e32 v7, v7
	s_addc_u32 s3, s5, 0
	global_load_dword v83, v79, s[2:3]
	s_lshl_b32 s2, s37, 8
	v_pk_add_f32 v[0:1], v[0:1], 1.0 op_sel_hi:[1,0]
	s_and_b32 s2, s2, 0xffff00
	s_nop 0
	s_nop 0
	v_exp_f32_e32 v16, v4
	v_exp_f32_e32 v17, v5
	v_log_f32_e32 v4, v0
	v_log_f32_e32 v5, v1
	s_nop 0
	s_nop 0
	s_add_u32 s2, s4, s2
	v_exp_f32_e32 v2, v2
	v_exp_f32_e32 v3, v3
	s_addc_u32 s3, s5, 0
	global_load_dword v92, v79, s[2:3]
	s_lshl_b32 s2, s21, 8
	v_pk_add_f32 v[6:7], v[6:7], 1.0 op_sel_hi:[1,0]
	s_and_b32 s2, s2, 0xffff00
	v_log_f32_e32 v6, v6
	v_log_f32_e32 v7, v7
	s_add_u32 s2, s4, s2
	v_pk_add_f32 v[0:1], v[16:17], 1.0 op_sel_hi:[1,0]
	s_addc_u32 s3, s5, 0
	global_load_dword v89, v79, s[2:3]
	s_lshl_b32 s2, s20, 8
	v_pk_add_f32 v[2:3], v[2:3], 1.0 op_sel_hi:[1,0]
	v_log_f32_e32 v0, v0
	v_log_f32_e32 v1, v1
	s_and_b32 s2, s2, 0xffff00
	v_exp_f32_e32 v18, v8
	v_exp_f32_e32 v19, v9
	v_log_f32_e32 v8, v2
	v_log_f32_e32 v9, v3
	s_add_u32 s2, s4, s2
	v_pk_mul_f32 v[2:3], v[48:49], v[6:7] op_sel:[1,0]
	s_nop 0
	s_nop 0
	s_addc_u32 s3, s5, 0
	s_lshl_b32 s19, s19, 8
	s_and_b32 s19, s19, 0xffff00
	v_pk_mul_f32 v[0:1], v[48:49], v[0:1] op_sel:[1,0]
	s_add_u32 s20, s4, s19
	s_nop 0
	s_nop 0
	v_cvt_pk_f16_f32 v3, v2, v3
	v_cvt_pk_f16_f32 v2, v0, v1
	v_pk_mul_f32 v[0:1], v[48:49], v[8:9] op_sel:[1,0]
	v_pk_mul_f32 v[4:5], v[48:49], v[4:5] op_sel:[1,0]
	s_addc_u32 s21, s5, 0
	s_lshl_b32 s18, s18, 8
	s_nop 0
	s_nop 0
	s_nop 0
	s_nop 0
	v_cvt_pk_f16_f32 v1, v0, v1
	v_cvt_pk_f16_f32 v0, v4, v5
	v_pk_add_f32 v[4:5], v[18:19], 1.0 op_sel_hi:[1,0]
	v_exp_f32_e32 v6, v10
	v_exp_f32_e32 v7, v11
	v_exp_f32_e32 v8, v12
	v_exp_f32_e32 v9, v13
	v_exp_f32_e32 v10, v14
	v_exp_f32_e32 v11, v15
	s_and_b32 s18, s18, 0xffff00
	s_add_u32 s18, s4, s18
	s_addc_u32 s19, s5, 0
	s_lshl_b32 s10, s10, 8
	s_and_b32 s10, s10, 0xffff00
	v_pk_add_f32 v[8:9], v[8:9], 1.0 op_sel_hi:[1,0]
	v_pk_add_f32 v[10:11], v[10:11], 1.0 op_sel_hi:[1,0]
	s_add_u32 s24, s4, s10
	v_pk_add_f32 v[6:7], v[6:7], 1.0 op_sel_hi:[1,0]
	v_log_f32_e32 v8, v8
	v_log_f32_e32 v9, v9
	v_log_f32_e32 v10, v10
	v_log_f32_e32 v11, v11
	s_addc_u32 s25, s5, 0
	global_load_dword v87, v79, s[2:3]
	global_load_dword v84, v79, s[20:21]
	global_load_dword v82, v79, s[18:19]
	global_load_dword v81, v79, s[24:25]
	ds_read_b128 v[12:15], v71
	v_log_f32_e32 v6, v6
	v_log_f32_e32 v7, v7
	v_log_f32_e32 v4, v4
	v_log_f32_e32 v5, v5
	v_pk_mul_f32 v[8:9], v[48:49], v[8:9] op_sel:[1,0]
	v_pk_mul_f32 v[10:11], v[48:49], v[10:11] op_sel:[1,0]
	v_cvt_pk_f16_f32 v118, v8, v9
	v_cvt_pk_f16_f32 v119, v10, v11
	v_pk_mul_f32 v[10:11], v[48:49], v[6:7] op_sel:[1,0]
	ds_read_b128 v[6:9], v71 offset:1024
	s_waitcnt lgkmcnt(1)
	v_mfma_f32_32x32x16_f16 v[16:31], v[0:3], v[12:15], 0
	s_nop 0
	s_nop 0
	v_mul_f32_e64 v4, v49, v4
	v_mul_f32_e64 v5, v49, v5
	v_exp_f32_e32 v32, v32
	v_exp_f32_e32 v33, v33
	s_nop 0
	s_nop 0
	v_cvt_pk_f16_f32 v117, v10, v11
	v_cvt_pk_f16_f32 v116, v4, v5
	v_exp_f32_e32 v36, v36
	v_exp_f32_e32 v37, v37
	v_pk_add_f32 v[32:33], v[32:33], 1.0 op_sel_hi:[1,0]
	s_waitcnt lgkmcnt(0)
	v_mfma_f32_32x32x16_f16 v[16:31], v[116:119], v[6:9], v[16:31]
	v_log_f32_e32 v54, v32
	v_log_f32_e32 v55, v33
	v_pk_add_f32 v[32:33], v[36:37], 1.0 op_sel_hi:[1,0]
	s_nop 0
	s_nop 0
	ds_read_b128 v[4:7], v71 offset:4096
	ds_read_b128 v[120:123], v71 offset:5120
	v_exp_f32_e32 v36, v38
	v_exp_f32_e32 v37, v39
	s_nop 0
	s_nop 0
	s_waitcnt lgkmcnt(1)
	v_mfma_f32_32x32x16_f16 v[0:15], v[0:3], v[4:7], 0
	v_exp_f32_e32 v34, v34
	v_exp_f32_e32 v35, v35
	v_pk_add_f32 v[36:37], v[36:37], 1.0 op_sel_hi:[1,0]
	v_log_f32_e32 v32, v32
	v_log_f32_e32 v33, v33
	v_log_f32_e32 v36, v36
	v_log_f32_e32 v37, v37
	v_pk_add_f32 v[34:35], v[34:35], 1.0 op_sel_hi:[1,0]
	v_pk_mul_f32 v[32:33], v[48:49], v[32:33] op_sel:[1,0]
	v_log_f32_e32 v38, v34
	v_log_f32_e32 v39, v35
	v_pk_mul_f32 v[34:35], v[48:49], v[36:37] op_sel:[1,0]
	v_pk_mul_f32 v[36:37], v[48:49], v[54:55] op_sel:[1,0]
	v_cvt_pk_f16_f32 v35, v34, v35
	v_cvt_pk_f16_f32 v34, v32, v33
	v_pk_mul_f32 v[32:33], v[48:49], v[38:39] op_sel:[1,0]
	s_waitcnt lgkmcnt(0)
	v_mfma_f32_32x32x16_f16 v[0:15], v[116:119], v[120:123], v[0:15]
	v_cvt_pk_f16_f32 v33, v32, v33
	v_cvt_pk_f16_f32 v32, v36, v37
	ds_read_b128 v[36:39], v71 offset:2048
	ds_read_b128 v[116:119], v71 offset:3072
	s_nop 0
	s_nop 0
	v_exp_f32_e32 v55, v44
	v_exp_f32_e32 v115, v45
	s_waitcnt lgkmcnt(1)
	v_mfma_f32_32x32x16_f16 v[16:31], v[32:35], v[36:39], v[16:31]
	ds_read_b128 v[36:39], v71 offset:6144
	v_exp_f32_e32 v44, v40
	v_exp_f32_e32 v45, v41
	v_exp_f32_e32 v52, v42
	v_exp_f32_e32 v54, v43
	ds_read_b128 v[40:43], v71 offset:7168
	s_nop 0
	s_waitcnt lgkmcnt(1)
	v_mfma_f32_32x32x16_f16 v[0:15], v[32:35], v[36:39], v[0:15]
	v_add_f32_e64 v34, v44, 1.0
	v_add_f32_e64 v35, v45, 1.0
	s_nop 0
	s_nop 0
	s_nop 0
	v_log_f32_e32 v36, v34
	v_log_f32_e32 v37, v35
	v_exp_f32_e32 v34, v46
	v_exp_f32_e32 v35, v47
	s_nop 0
	s_nop 0
	v_add_f32_e64 v32, v55, 1.0
	v_add_f32_e64 v33, v115, 1.0
	v_pk_add_f32 v[34:35], v[34:35], 1.0 op_sel_hi:[1,0]
	v_log_f32_e32 v32, v32
	v_log_f32_e32 v33, v33
	v_log_f32_e32 v34, v34
	v_log_f32_e32 v35, v35
	v_add_f32_e64 v38, v52, 1.0
	v_add_f32_e64 v39, v54, 1.0
	v_pk_mul_f32 v[32:33], v[48:49], v[32:33] op_sel:[1,0]
	v_log_f32_e32 v38, v38
	v_log_f32_e32 v39, v39
	v_pk_mul_f32 v[34:35], v[48:49], v[34:35] op_sel:[1,0]
	v_pk_mul_f32 v[36:37], v[48:49], v[36:37] op_sel:[1,0]
	v_cvt_pk_f16_f32 v35, v34, v35
	v_cvt_pk_f16_f32 v34, v32, v33
	v_pk_mul_f32 v[32:33], v[48:49], v[38:39] op_sel:[1,0]
	v_mov_b32_e32 v54, v53
	v_cvt_pk_f16_f32 v33, v32, v33
	v_cvt_pk_f16_f32 v32, v36, v37
	v_cvt_f16_f32_e32 v36, v49
	v_mov_b32_e32 v55, v53
	v_mfma_f32_32x32x16_f16 v[16:31], v[32:35], v[116:119], v[16:31]
	v_cmp_ne_u32_sdwa s[20:21], v95, v50 src0_sel:DWORD src1_sel:WORD_1
	v_cmp_ne_u32_sdwa s[18:19], v99, v50 src0_sel:WORD_1 src1_sel:WORD_1
	s_bitcmp1_b32 s20, 0
	v_cmp_lt_i32_e64 s[2:3], s13, v64
	s_cselect_b64 s[20:21], -1, 0
	s_bitcmp0_b32 s18, 0
	s_waitcnt lgkmcnt(0)
	v_mfma_f32_32x32x16_f16 v[0:15], v[32:35], v[40:43], v[0:15]
	v_cndmask_b32_e64 v32, 0, v36, s[0:1]
	v_pack_b32_f16 v52, v32, 0
	ds_read_b128 v[32:35], v72
	ds_read_b128 v[36:39], v72 offset:1024
	s_waitcnt vmcnt(0)
	s_waitcnt vmcnt(0)
	s_waitcnt lgkmcnt(1)
	v_mfma_f32_32x32x16_f16 v[16:31], v[52:55], v[32:35], v[16:31]
	v_mov_b64_e32 v[32:33], 0
	s_nop 0
	s_waitcnt lgkmcnt(0)
	v_mfma_f32_32x32x16_f16 v[0:15], v[52:55], v[36:39], v[0:15]
	s_nop 11
	v_permlane32_swap_b32_e32 v16, v0
	v_permlane32_swap_b32_e32 v17, v1
	v_permlane32_swap_b32_e32 v18, v2
	v_permlane32_swap_b32_e32 v19, v3
	v_permlane32_swap_b32_e32 v20, v4
	v_permlane32_swap_b32_e32 v21, v5
	v_permlane32_swap_b32_e32 v22, v6
	v_permlane32_swap_b32_e32 v23, v7
	v_permlane32_swap_b32_e32 v24, v8
	v_permlane32_swap_b32_e32 v25, v9
	v_permlane32_swap_b32_e32 v26, v10
	v_permlane32_swap_b32_e32 v27, v11
	v_permlane32_swap_b32_e32 v28, v12
	v_permlane32_swap_b32_e32 v29, v13
	v_permlane32_swap_b32_e32 v30, v14
	v_permlane32_swap_b32_e32 v31, v15
	v_fma_mix_f32 v32, v16, v112, v32 op_sel:[0,1,0] op_sel_hi:[0,1,0]
	v_fma_mix_f32 v33, v16, v112, v33 op_sel_hi:[0,1,0]
	s_cbranch_scc1 .LBB4_13
	v_readlane_b32 s10, v50, 0
	s_bfe_u32 s19, s10, 0x80008
	v_lshl_or_b32 v16, s19, 7, v73
	ds_read_u16 v16, v16
	s_bfe_u32 s10, s10, 0x100010
	s_lshl_b32 s10, s10, 8
	s_add_u32 s58, s60, s10
	s_addc_u32 s59, s61, 0
	s_cmp_lg_u64 s[20:21], 0
	s_cselect_b32 s58, s58, s62
	s_cselect_b32 s59, s59, s63
	s_nop 0
	s_waitcnt lgkmcnt(0)
	v_fma_mix_f32 v16, v16, v33, v32 op_sel_hi:[1,0,0]
	s_nop 0
	s_mov_b64 s[20:21], -1
	v_mov_b64_e32 v[32:33], 0
	s_nop 0
	global_store_dword v79, v16, s[58:59] sc1

	.amdhsa_kernel _Z7k_edge1PK15HIP_vector_typeIfLj4EEPKDv8_DF16_S5_PKfS7_S7_PKDv2_DF16_PfSB_
		.amdhsa_group_segment_fixed_size 31488
		.amdhsa_private_segment_fixed_size 0
		.amdhsa_kernarg_size 328
		.amdhsa_user_sgpr_count 2
		.amdhsa_user_sgpr_dispatch_ptr 0
		.amdhsa_user_sgpr_queue_ptr 0
		.amdhsa_user_sgpr_kernarg_segment_ptr 1
		.amdhsa_user_sgpr_dispatch_id 0
		.amdhsa_user_sgpr_kernarg_preload_length 0
		.amdhsa_user_sgpr_kernarg_preload_offset 0
		.amdhsa_user_sgpr_private_segment_size 0
		.amdhsa_uses_dynamic_stack 0
		.amdhsa_enable_private_segment 0
		.amdhsa_system_sgpr_workgroup_id_x 1
		.amdhsa_system_sgpr_workgroup_id_y 0
		.amdhsa_system_sgpr_workgroup_id_z 0
		.amdhsa_system_sgpr_workgroup_info 0
		.amdhsa_system_vgpr_workitem_id 0
		.amdhsa_next_free_vgpr 128
		.amdhsa_next_free_sgpr 96
		.amdhsa_accum_offset 128
		.amdhsa_reserve_vcc 1
		.amdhsa_float_round_mode_32 0
		.amdhsa_float_round_mode_16_64 0
		.amdhsa_float_denorm_mode_32 3
		.amdhsa_float_denorm_mode_16_64 3
		.amdhsa_dx10_clamp 1
		.amdhsa_ieee_mode 1
		.amdhsa_fp16_overflow 0
		.amdhsa_tg_split 0
		.amdhsa_exception_fp_ieee_invalid_op 0
		.amdhsa_exception_fp_denorm_src 0
		.amdhsa_exception_fp_ieee_div_zero 0
		.amdhsa_exception_fp_ieee_overflow 0
		.amdhsa_exception_fp_ieee_underflow 0
		.amdhsa_exception_fp_ieee_inexact 0
		.amdhsa_exception_int_div_zero 0
	.end_amdhsa_kernel

amdhsa.kernels:
  - .agpr_count:     0
    .args:
      - .actual_access:  read_only
        .address_space:  global
        .offset:         0
        .size:           8
        .value_kind:     global_buffer
      - .actual_access:  write_only
        .address_space:  global
        .offset:         8
        .size:           8
        .value_kind:     global_buffer
      - .offset:         16
        .size:           288
        .value_kind:     by_value
      - .actual_access:  write_only
        .address_space:  global
        .offset:         304
        .size:           8
        .value_kind:     global_buffer
      - .actual_access:  write_only
        .address_space:  global
        .offset:         312
        .size:           8
        .value_kind:     global_buffer
    .group_segment_fixed_size: 1564
    .kernarg_segment_align: 8
    .kernarg_segment_size: 320
    .language:       OpenCL C
    .language_version:
      - 2
      - 0
    .max_flat_workgroup_size: 256
    .name:           _Z8k_bcountPKiPi8PrepArgsPDF16_S3_
    .private_segment_fixed_size: 0
    .sgpr_count:     26
    .sgpr_spill_count: 0
    .symbol:         _Z8k_bcountPKiPi8PrepArgsPDF16_S3_.kd
    .uniform_work_group_size: 1
    .uses_dynamic_stack: false
    .vgpr_count:     26
    .vgpr_spill_count: 0
    .wavefront_size: 64
  - .agpr_count:     0
    .args:
      - .actual_access:  read_only
        .address_space:  global
        .offset:         0
        .size:           8
        .value_kind:     global_buffer
      - .actual_access:  read_only
        .address_space:  global
        .offset:         8
        .size:           8
        .value_kind:     global_buffer
      - .actual_access:  read_only
        .address_space:  global
        .offset:         16
        .size:           8
        .value_kind:     global_buffer
      - .actual_access:  read_only
        .address_space:  global
        .offset:         24
        .size:           8
        .value_kind:     global_buffer
      - .actual_access:  write_only
        .address_space:  global
        .offset:         32
        .size:           8
        .value_kind:     global_buffer
      - .actual_access:  write_only
        .address_space:  global
        .offset:         40
        .size:           8
        .value_kind:     global_buffer
      - .actual_access:  write_only
        .address_space:  global
        .offset:         48
        .size:           8
        .value_kind:     global_buffer
    .group_segment_fixed_size: 19228
    .kernarg_segment_align: 8
    .kernarg_segment_size: 56
    .language:       OpenCL C
    .language_version:
      - 2
      - 0
    .max_flat_workgroup_size: 512
    .name:           _Z10k_bscatterPKfPKiS2_S2_PiP15HIP_vector_typeIfLj2EEPf
    .private_segment_fixed_size: 0
    .sgpr_count:     22
    .sgpr_spill_count: 0
    .symbol:         _Z10k_bscatterPKfPKiS2_S2_PiP15HIP_vector_typeIfLj2EEPf.kd
    .uniform_work_group_size: 1
    .uses_dynamic_stack: false
    .vgpr_count:     67
    .vgpr_spill_count: 0
    .wavefront_size: 64
  - .agpr_count:     0
    .args:
      - .actual_access:  read_only
        .address_space:  global
        .offset:         0
        .size:           8
        .value_kind:     global_buffer
      - .actual_access:  read_only
        .address_space:  global
        .offset:         8
        .size:           8
        .value_kind:     global_buffer
      - .actual_access:  read_only
        .address_space:  global
        .offset:         16
        .size:           8
        .value_kind:     global_buffer
      - .actual_access:  write_only
        .address_space:  global
        .offset:         24
        .size:           8
        .value_kind:     global_buffer
      - .actual_access:  write_only
        .address_space:  global
        .offset:         32
        .size:           8
        .value_kind:     global_buffer
    .group_segment_fixed_size: 1024
    .kernarg_segment_align: 8
    .kernarg_segment_size: 40
    .language:       OpenCL C
    .language_version:
      - 2
      - 0
    .max_flat_workgroup_size: 512
    .name:           _Z7k_bsortPK15HIP_vector_typeIfLj2EEPKiS4_PS_IfLj4EEPi
    .private_segment_fixed_size: 0
    .sgpr_count:     56
    .sgpr_spill_count: 0
    .symbol:         _Z7k_bsortPK15HIP_vector_typeIfLj2EEPKiS4_PS_IfLj4EEPi.kd
    .uniform_work_group_size: 1
    .uses_dynamic_stack: false
    .vgpr_count:     64
    .vgpr_spill_count: 0
    .wavefront_size: 64
  - .agpr_count:     0
    .args:
      - .actual_access:  read_only
        .address_space:  global
        .offset:         0
        .size:           8
        .value_kind:     global_buffer
      - .actual_access:  read_only
        .address_space:  global
        .offset:         8
        .size:           8
        .value_kind:     global_buffer
      - .actual_access:  read_only
        .address_space:  global
        .offset:         16
        .size:           8
        .value_kind:     global_buffer
      - .actual_access:  read_only
        .address_space:  global
        .offset:         24
        .size:           8
        .value_kind:     global_buffer
      - .actual_access:  read_only
        .address_space:  global
        .offset:         32
        .size:           8
        .value_kind:     global_buffer
      - .actual_access:  read_only
        .address_space:  global
        .offset:         40
        .size:           8
        .value_kind:     global_buffer
      - .actual_access:  write_only
        .address_space:  global
        .offset:         48
        .size:           8
        .value_kind:     global_buffer
      - .actual_access:  write_only
        .address_space:  global
        .offset:         56
        .size:           8
        .value_kind:     global_buffer
      - .offset:         64
        .size:           4
        .value_kind:     hidden_block_count_x
      - .offset:         68
        .size:           4
        .value_kind:     hidden_block_count_y
      - .offset:         72
        .size:           4
        .value_kind:     hidden_block_count_z
      - .offset:         76
        .size:           2
        .value_kind:     hidden_group_size_x
      - .offset:         78
        .size:           2
        .value_kind:     hidden_group_size_y
      - .offset:         80
        .size:           2
        .value_kind:     hidden_group_size_z
      - .offset:         82
        .size:           2
        .value_kind:     hidden_remainder_x
      - .offset:         84
        .size:           2
        .value_kind:     hidden_remainder_y
      - .offset:         86
        .size:           2
        .value_kind:     hidden_remainder_z
      - .offset:         104
        .size:           8
        .value_kind:     hidden_global_offset_x
      - .offset:         112
        .size:           8
        .value_kind:     hidden_global_offset_y
      - .offset:         120
        .size:           8
        .value_kind:     hidden_global_offset_z
      - .offset:         128
        .size:           2
        .value_kind:     hidden_grid_dims
    .group_segment_fixed_size: 31488
    .kernarg_segment_align: 8
    .kernarg_segment_size: 320
    .language:       OpenCL C
    .language_version:
      - 2
      - 0
    .max_flat_workgroup_size: 256
    .name:           _Z7k_edge0PK15HIP_vector_typeIfLj4EEPKDv8_DF16_S5_PKfS7_S7_PfS8_
    .private_segment_fixed_size: 0
    .sgpr_count:     59
    .sgpr_spill_count: 0
    .symbol:         _Z7k_edge0PK15HIP_vector_typeIfLj4EEPKDv8_DF16_S5_PKfS7_S7_PfS8_.kd
    .uniform_work_group_size: 1
    .uses_dynamic_stack: false
    .vgpr_count:     96
    .vgpr_spill_count: 0
    .wavefront_size: 64
  - .agpr_count:     0
    .args:
      - .actual_access:  read_only
        .address_space:  global
        .offset:         0
        .size:           8
        .value_kind:     global_buffer
      - .actual_access:  read_only
        .address_space:  global
        .offset:         8
        .size:           8
        .value_kind:     global_buffer
      - .actual_access:  read_only
        .address_space:  global
        .offset:         16
        .size:           8
        .value_kind:     global_buffer
      - .actual_access:  read_only
        .address_space:  global
        .offset:         24
        .size:           8
        .value_kind:     global_buffer
      - .actual_access:  read_only
        .address_space:  global
        .offset:         32
        .size:           8
        .value_kind:     global_buffer
      - .actual_access:  read_only
        .address_space:  global
        .offset:         40
        .size:           8
        .value_kind:     global_buffer
      - .address_space:  global
        .offset:         48
        .size:           8
        .value_kind:     global_buffer
      - .actual_access:  write_only
        .address_space:  global
        .offset:         56
        .size:           8
        .value_kind:     global_buffer
      - .actual_access:  write_only
        .address_space:  global
        .offset:         64
        .size:           8
        .value_kind:     global_buffer
      - .offset:         72
        .size:           4
        .value_kind:     hidden_block_count_x
      - .offset:         76
        .size:           4
        .value_kind:     hidden_block_count_y
      - .offset:         80
        .size:           4
        .value_kind:     hidden_block_count_z
      - .offset:         84
        .size:           2
        .value_kind:     hidden_group_size_x
      - .offset:         86
        .size:           2
        .value_kind:     hidden_group_size_y
      - .offset:         88
        .size:           2
        .value_kind:     hidden_group_size_z
      - .offset:         90
        .size:           2
        .value_kind:     hidden_remainder_x
      - .offset:         92
        .size:           2
        .value_kind:     hidden_remainder_y
      - .offset:         94
        .size:           2
        .value_kind:     hidden_remainder_z
      - .offset:         112
        .size:           8
        .value_kind:     hidden_global_offset_x
      - .offset:         120
        .size:           8
        .value_kind:     hidden_global_offset_y
      - .offset:         128
        .size:           8
        .value_kind:     hidden_global_offset_z
      - .offset:         136
        .size:           2
        .value_kind:     hidden_grid_dims
    .group_segment_fixed_size: 31488
    .kernarg_segment_align: 8
    .kernarg_segment_size: 328
    .language:       OpenCL C
    .language_version:
      - 2
      - 0
    .max_flat_workgroup_size: 256
    .name:           _Z7k_edge1PK15HIP_vector_typeIfLj4EEPKDv8_DF16_S5_PKfS7_S7_PKDv2_DF16_PfSB_
    .private_segment_fixed_size: 0
    .sgpr_count:     56
    .sgpr_spill_count: 0
    .symbol:         _Z7k_edge1PK15HIP_vector_typeIfLj4EEPKDv8_DF16_S5_PKfS7_S7_PKDv2_DF16_PfSB_.kd
    .uniform_work_group_size: 1
    .uses_dynamic_stack: false
    .vgpr_count:     128
    .vgpr_spill_count: 0
    .wavefront_size: 64
  - .agpr_count:     0
    .args:
      - .actual_access:  read_only
        .address_space:  global
        .offset:         0
        .size:           8
        .value_kind:     global_buffer
      - .actual_access:  read_only
        .address_space:  global
        .offset:         8
        .size:           8
        .value_kind:     global_buffer
      - .address_space:  global
        .offset:         16
        .size:           8
        .value_kind:     global_buffer
      - .address_space:  global
        .offset:         24
        .size:           8
        .value_kind:     global_buffer
    .group_segment_fixed_size: 0
    .kernarg_segment_align: 8
    .kernarg_segment_size: 32
    .language:       OpenCL C
    .language_version:
      - 2
      - 0
    .max_flat_workgroup_size: 256
    .name:           _Z6k_poolPKfPKiPfS3_
    .private_segment_fixed_size: 0
    .sgpr_count:     20
    .sgpr_spill_count: 0
    .symbol:         _Z6k_poolPKfPKiPfS3_.kd
    .uniform_work_group_size: 1
    .uses_dynamic_stack: false
    .vgpr_count:     16
    .vgpr_spill_count: 0
    .wavefront_size: 64
  - .agpr_count:     0
    .args:
      - .actual_access:  read_only
        .address_space:  global
        .offset:         0
        .size:           8
        .value_kind:     global_buffer
      - .actual_access:  read_only
        .address_space:  global
        .offset:         8
        .size:           8
        .value_kind:     global_buffer
      - .actual_access:  read_only
        .address_space:  global
        .offset:         16
        .size:           8
        .value_kind:     global_buffer
      - .actual_access:  read_only
        .address_space:  global
        .offset:         24
        .size:           8
        .value_kind:     global_buffer
      - .actual_access:  read_only
        .address_space:  global
        .offset:         32
        .size:           8
        .value_kind:     global_buffer
      - .actual_access:  read_only
        .address_space:  global
        .offset:         40
        .size:           8
        .value_kind:     global_buffer
      - .actual_access:  write_only
        .address_space:  global
        .offset:         48
        .size:           8
        .value_kind:     global_buffer
    .group_segment_fixed_size: 20480
    .kernarg_segment_align: 8
    .kernarg_segment_size: 56
    .language:       OpenCL C
    .language_version:
      - 2
      - 0
    .max_flat_workgroup_size: 64
    .name:           _Z7k_finalPKfS0_S0_S0_S0_S0_Pf
    .private_segment_fixed_size: 0
    .sgpr_count:     42
    .sgpr_spill_count: 0
    .symbol:         _Z7k_finalPKfS0_S0_S0_S0_S0_Pf.kd
    .uniform_work_group_size: 1
    .uses_dynamic_stack: false
    .vgpr_count:     144
    .vgpr_spill_count: 0
    .wavefront_size: 64
  - .agpr_count:     0
    .args:
      - .actual_access:  read_only
        .address_space:  global
        .offset:         0
        .size:           8
        .value_kind:     global_buffer
      - .address_space:  global
        .offset:         8
        .size:           8
        .value_kind:     global_buffer
      - .address_space:  global
        .offset:         16
        .size:           8
        .value_kind:     global_buffer
      - .actual_access:  read_only
        .address_space:  global
        .offset:         24
        .size:           8
        .value_kind:     global_buffer
      - .actual_access:  read_only
        .address_space:  global
        .offset:         32
        .size:           8
        .value_kind:     global_buffer
      - .actual_access:  read_only
        .address_space:  global
        .offset:         40
        .size:           8
        .value_kind:     global_buffer
      - .actual_access:  read_only
        .address_space:  global
        .offset:         48
        .size:           8
        .value_kind:     global_buffer
      - .actual_access:  read_only
        .address_space:  global
        .offset:         56
        .size:           8
        .value_kind:     global_buffer
      - .actual_access:  read_only
        .address_space:  global
        .offset:         64
        .size:           8
        .value_kind:     global_buffer
      - .actual_access:  read_only
        .address_space:  global
        .offset:         72
        .size:           8
        .value_kind:     global_buffer
      - .actual_access:  read_only
        .address_space:  global
        .offset:         80
        .size:           8
        .value_kind:     global_buffer
      - .actual_access:  read_only
        .address_space:  global
        .offset:         88
        .size:           8
        .value_kind:     global_buffer
      - .actual_access:  read_only
        .address_space:  global
        .offset:         96
        .size:           8
        .value_kind:     global_buffer
      - .actual_access:  read_only
        .address_space:  global
        .offset:         104
        .size:           8
        .value_kind:     global_buffer
      - .actual_access:  read_only
        .address_space:  global
        .offset:         112
        .size:           8
        .value_kind:     global_buffer
    .group_segment_fixed_size: 59392
    .kernarg_segment_align: 8
    .kernarg_segment_size: 120
    .language:       OpenCL C
    .language_version:
      - 2
      - 0
    .max_flat_workgroup_size: 256
    .name:           _Z6k_nodeILi0ELi0EEvPfS0_PDv2_DF16_PKiPKfS4_S0_S0_S4_S6_PKDv8_DF16_S6_S9_S6_S9_
    .private_segment_fixed_size: 0
    .sgpr_count:     30
    .sgpr_spill_count: 0
    .symbol:         _Z6k_nodeILi0ELi0EEvPfS0_PDv2_DF16_PKiPKfS4_S0_S0_S4_S6_PKDv8_DF16_S6_S9_S6_S9_.kd
    .uniform_work_group_size: 1
    .uses_dynamic_stack: false
    .vgpr_count:     154
    .vgpr_spill_count: 0
    .wavefront_size: 64
  - .agpr_count:     0
    .args:
      - .actual_access:  read_only
        .address_space:  global
        .offset:         0
        .size:           8
        .value_kind:     global_buffer
      - .address_space:  global
        .offset:         8
        .size:           8
        .value_kind:     global_buffer
      - .address_space:  global
        .offset:         16
        .size:           8
        .value_kind:     global_buffer
      - .actual_access:  read_only
        .address_space:  global
        .offset:         24
        .size:           8
        .value_kind:     global_buffer
      - .actual_access:  read_only
        .address_space:  global
        .offset:         32
        .size:           8
        .value_kind:     global_buffer
      - .actual_access:  read_only
        .address_space:  global
        .offset:         40
        .size:           8
        .value_kind:     global_buffer
      - .actual_access:  read_only
        .address_space:  global
        .offset:         48
        .size:           8
        .value_kind:     global_buffer
      - .actual_access:  read_only
        .address_space:  global
        .offset:         56
        .size:           8
        .value_kind:     global_buffer
      - .actual_access:  read_only
        .address_space:  global
        .offset:         64
        .size:           8
        .value_kind:     global_buffer
      - .actual_access:  read_only
        .address_space:  global
        .offset:         72
        .size:           8
        .value_kind:     global_buffer
      - .actual_access:  read_only
        .address_space:  global
        .offset:         80
        .size:           8
        .value_kind:     global_buffer
      - .actual_access:  read_only
        .address_space:  global
        .offset:         88
        .size:           8
        .value_kind:     global_buffer
      - .actual_access:  read_only
        .address_space:  global
        .offset:         96
        .size:           8
        .value_kind:     global_buffer
      - .actual_access:  read_only
        .address_space:  global
        .offset:         104
        .size:           8
        .value_kind:     global_buffer
      - .actual_access:  read_only
        .address_space:  global
        .offset:         112
        .size:           8
        .value_kind:     global_buffer
    .group_segment_fixed_size: 59392
    .kernarg_segment_align: 8
    .kernarg_segment_size: 120
    .language:       OpenCL C
    .language_version:
      - 2
      - 0
    .max_flat_workgroup_size: 256
    .name:           _Z6k_nodeILi1ELi0EEvPfS0_PDv2_DF16_PKiPKfS4_S0_S0_S4_S6_PKDv8_DF16_S6_S9_S6_S9_
    .private_segment_fixed_size: 0
    .sgpr_count:     30
    .sgpr_spill_count: 0
    .symbol:         _Z6k_nodeILi1ELi0EEvPfS0_PDv2_DF16_PKiPKfS4_S0_S0_S4_S6_PKDv8_DF16_S6_S9_S6_S9_.kd
    .uniform_work_group_size: 1
    .uses_dynamic_stack: false
    .vgpr_count:     220
    .vgpr_spill_count: 0
    .wavefront_size: 64
  - .agpr_count:     0
    .args:
      - .actual_access:  read_only
        .address_space:  global
        .offset:         0
        .size:           8
        .value_kind:     global_buffer
      - .actual_access:  read_only
        .address_space:  global
        .offset:         8
        .size:           8
        .value_kind:     global_buffer
      - .address_space:  global
        .offset:         16
        .size:           8
        .value_kind:     global_buffer
      - .actual_access:  read_only
        .address_space:  global
        .offset:         24
        .size:           8
        .value_kind:     global_buffer
      - .actual_access:  read_only
        .address_space:  global
        .offset:         32
        .size:           8
        .value_kind:     global_buffer
      - .actual_access:  read_only
        .address_space:  global
        .offset:         40
        .size:           8
        .value_kind:     global_buffer
      - .address_space:  global
        .offset:         48
        .size:           8
        .value_kind:     global_buffer
      - .address_space:  global
        .offset:         56
        .size:           8
        .value_kind:     global_buffer
      - .actual_access:  read_only
        .address_space:  global
        .offset:         64
        .size:           8
        .value_kind:     global_buffer
      - .actual_access:  read_only
        .address_space:  global
        .offset:         72
        .size:           8
        .value_kind:     global_buffer
      - .actual_access:  read_only
        .address_space:  global
        .offset:         80
        .size:           8
        .value_kind:     global_buffer
      - .actual_access:  read_only
        .address_space:  global
        .offset:         88
        .size:           8
        .value_kind:     global_buffer
      - .actual_access:  read_only
        .address_space:  global
        .offset:         96
        .size:           8
        .value_kind:     global_buffer
      - .actual_access:  read_only
        .address_space:  global
        .offset:         104
        .size:           8
        .value_kind:     global_buffer
      - .actual_access:  read_only
        .address_space:  global
        .offset:         112
        .size:           8
        .value_kind:     global_buffer
    .group_segment_fixed_size: 59392
    .kernarg_segment_align: 8
    .kernarg_segment_size: 120
    .language:       OpenCL C
    .language_version:
      - 2
      - 0
    .max_flat_workgroup_size: 256
    .name:           _Z6k_nodeILi1ELi1EEvPfS0_PDv2_DF16_PKiPKfS4_S0_S0_S4_S6_PKDv8_DF16_S6_S9_S6_S9_
    .private_segment_fixed_size: 0
    .sgpr_count:     30
    .sgpr_spill_count: 0
    .symbol:         _Z6k_nodeILi1ELi1EEvPfS0_PDv2_DF16_PKiPKfS4_S0_S0_S4_S6_PKDv8_DF16_S6_S9_S6_S9_.kd
    .uniform_work_group_size: 1
    .uses_dynamic_stack: false
    .vgpr_count:     220
    .vgpr_spill_count: 0
    .wavefront_size: 64
